# baseline (speedup 1.0000x reference)
_Z11lstm_kernelPKiPKhPKfS4_S4_Pf:
	s_load_dwordx4 s[12:15], s[0:1], 0x0
	v_readfirstlane_b32 s19, v0
	v_or_b32_e32 v3, 0x400, v0
	s_movk_i32 s4, 0x500
	s_lshr_b32 s7, s19, 6
	s_lshl_b32 s18, s2, 6
	s_mulk_i32 s2, 0x1400
	v_mov_b32_e32 v2, 0x4ff
	v_cmp_gt_u32_e32 vcc, s4, v3
	s_mul_hi_i32 s3, s18, 0x50
	s_waitcnt lgkmcnt(0)
	s_add_u32 s2, s12, s2
	v_cndmask_b32_e32 v2, v2, v3, vcc
	s_addc_u32 s3, s13, s3
	v_lshlrev_b32_e32 v1, 2, v0
	v_lshlrev_b32_e32 v4, 2, v2
	s_movk_i32 s4, 0x184
	v_or_b32_e32 v28, 0x200, v0
	global_load_dword v29, v1, s[2:3]
	global_load_dword v30, v1, s[2:3] offset:2048
	global_load_dword v2, v4, s[2:3]
	v_mov_b32_e32 v4, 0x383
	v_cmp_gt_u32_e32 vcc, s4, v0
	s_add_u32 s2, s14, 0x34000
	s_addc_u32 s3, s15, 0
	v_cndmask_b32_e32 v4, v4, v28, vcc
	v_lshlrev_b32_e32 v31, 4, v0
	v_lshlrev_b32_e32 v4, 4, v4
	global_load_dwordx4 v[6:9], v31, s[2:3]
	global_load_dwordx4 v[10:13], v4, s[2:3]
	v_and_b32_e32 v4, 0x7f, v0
	v_lshlrev_b32_e32 v18, 4, v4
	v_mov_b32_e32 v19, 0
	v_lshl_add_u64 v[4:5], s[14:15], 0, v[18:19]
	s_mov_b32 s2, 0x37000
	v_add_co_u32_e64 v4, s[2:3], s2, v4
	s_nop 1
	v_addc_co_u32_e64 v5, s[2:3], 0, v5, s[2:3]
	global_load_dwordx4 v[14:17], v[4:5], off offset:2112
	s_movk_i32 s22, 0x410
	s_movk_i32 s2, 0x4ff
	v_and_b32_e32 v4, 63, v0
	v_cmp_lt_u32_e64 s[2:3], s2, v3
	s_mul_i32 s5, s7, 0x6000
	s_mul_hi_u32 s4, s7, 0x6000
	s_add_u32 s8, s14, s5
	s_addc_u32 s9, s15, s4
	v_lshlrev_b32_e32 v210, 4, v4
	v_mov_b32_e32 v211, v19
	v_lshl_add_u64 v[20:21], s[8:9], 0, v[210:211]
	s_movk_i32 s4, 0x2000
	v_add_co_u32_e64 v22, s[4:5], s4, v20
	s_nop 1
	v_addc_co_u32_e64 v23, s[4:5], 0, v21, s[4:5]
	s_movk_i32 s4, 0x3000
	s_nop 0
	v_add_co_u32_e64 v24, s[4:5], s4, v20
	global_load_dwordx4 v[90:93], v[22:23], off offset:1024
	global_load_dwordx4 v[86:89], v[22:23], off offset:2048
	v_addc_co_u32_e64 v25, s[4:5], 0, v21, s[4:5]
	s_movk_i32 s4, 0x5000
	s_nop 0
	v_add_co_u32_e64 v26, s[4:5], s4, v20
	s_nop 1
	v_addc_co_u32_e64 v27, s[4:5], 0, v21, s[4:5]
	global_load_dwordx4 v[82:85], v[22:23], off offset:3072
	global_load_dwordx4 v[46:49], v[26:27], off
	global_load_dwordx4 v[42:45], v[26:27], off offset:1024
	global_load_dwordx4 v[38:41], v[26:27], off offset:2048
	global_load_dwordx4 v[94:97], v[24:25], off offset:-4096
	global_load_dwordx4 v[34:37], v[26:27], off offset:3072
	s_movk_i32 s4, 0x1000
	v_add_co_u32_e64 v22, s[4:5], s4, v20
	global_load_dwordx4 v[126:129], v210, s[8:9]
	global_load_dwordx4 v[122:125], v210, s[8:9] offset:1024
	global_load_dwordx4 v[118:121], v210, s[8:9] offset:2048
	global_load_dwordx4 v[114:117], v210, s[8:9] offset:3072
	v_addc_co_u32_e64 v23, s[4:5], 0, v21, s[4:5]
	global_load_dwordx4 v[110:113], v[22:23], off
	global_load_dwordx4 v[106:109], v[22:23], off offset:1024
	global_load_dwordx4 v[102:105], v[22:23], off offset:2048
	global_load_dwordx4 v[98:101], v[22:23], off offset:3072
	global_load_dwordx4 v[78:81], v[24:25], off
	global_load_dwordx4 v[74:77], v[24:25], off offset:1024
	global_load_dwordx4 v[70:73], v[24:25], off offset:2048
	global_load_dwordx4 v[66:69], v[24:25], off offset:3072
	s_movk_i32 s4, 0x4000
	v_add_co_u32_e64 v20, s[4:5], s4, v20
	v_mov_b32_e32 v5, 0x4000
	s_nop 0
	v_addc_co_u32_e64 v21, s[4:5], 0, v21, s[4:5]
	global_load_dwordx4 v[62:65], v[20:21], off
	global_load_dwordx4 v[58:61], v[20:21], off offset:1024
	global_load_dwordx4 v[54:57], v[20:21], off offset:2048
	global_load_dwordx4 v[50:53], v[20:21], off offset:3072
	s_waitcnt vmcnt(26)
	ds_write_b128 v31, v[6:9] offset:16384
	v_lshl_or_b32 v5, v28, 4, v5
	v_add_u32_e32 v6, 0x9840, v31
	v_cndmask_b32_e32 v5, v6, v5, vcc
	s_waitcnt vmcnt(25)
	ds_write_b128 v5, v[10:13]
	s_waitcnt vmcnt(24)
	ds_write_b128 v18, v[14:17] offset:36928
	v_mul_u32_u24_e32 v5, 0xccd, v0
	v_lshrrev_b32_e32 v5, 16, v5
	s_mov_b32 s5, 0xffffec
	v_mul_u32_u24_e32 v6, 0xccd, v28
	s_movk_i32 s4, 0x90
	v_mad_u32_u24 v8, v5, s5, v0
	v_lshlrev_b32_e32 v5, 2, v5
	v_lshrrev_b32_e32 v6, 16, v6
	v_mul_lo_u32 v7, v29, s4
	v_lshl_or_b32 v5, v8, 8, v5
	ds_write_b32 v5, v7 offset:30784
	v_mul_lo_u32 v196, v29, s22
	v_add_u32_e32 v197, 0x24e80, v5
	ds_write_b32 v197, v196
	v_mad_u32_u24 v7, v6, s5, v28
	v_lshlrev_b32_e32 v6, 2, v6
	v_mul_lo_u32 v5, v30, s4
	v_lshl_or_b32 v6, v7, 8, v6
	ds_write_b32 v6, v5 offset:30784
	v_mul_lo_u32 v198, v30, s22
	v_add_u32_e32 v199, 0x24e80, v6
	ds_write_b32 v199, v198
	s_and_saveexec_b64 s[4:5], s[2:3]
	s_xor_b64 s[2:3], exec, s[4:5]
	v_mov_b32_e32 v3, 0x9840
	v_lshl_add_u32 v5, v0, 2, v3
	s_andn2_saveexec_b64 s[2:3], s[2:3]
	v_mul_u32_u24_e32 v5, 0xccd, v3
	s_mov_b32 s4, 0xffffec
	v_mul_u32_u24_sdwa v6, v5, s4 dst_sel:DWORD dst_unused:UNUSED_PAD src0_sel:WORD_1 src1_sel:DWORD
	v_add_lshl_u32 v3, v6, v3, 8
	v_mov_b32_e32 v6, 2
	v_lshlrev_b32_sdwa v5, v6, v5 dst_sel:DWORD dst_unused:UNUSED_PAD src0_sel:DWORD src1_sel:WORD_1
	s_movk_i32 s4, 0x7840
	v_add3_u32 v5, v5, v3, s4
	s_or_b64 exec, exec, s[2:3]
	v_lshrrev_b32_e32 v3, 5, v4
	s_movk_i32 s2, 0x90
	s_lshl_b32 s6, s7, 10
	s_mulk_i32 s7, 0xfd00
	v_and_b32_e32 v182, 31, v0
	v_mul_lo_u32 v200, v2, s22
	v_mul_lo_u32 v2, v2, s2
	s_add_i32 s7, s6, s7
	v_lshlrev_b32_e32 v229, 6, v3
	ds_write_b32 v5, v2
	v_add_u32_e32 v201, 0x1d640, v5
	ds_write_b32 v201, v200
	v_lshlrev_b32_e32 v230, 4, v3
	v_lshlrev_b32_e32 v228, 2, v182
	v_or_b32_e32 v2, s7, v229
	s_waitcnt lgkmcnt(0)
	s_barrier
	s_cmpk_lt_u32 s19, 0x100
	s_cbranch_scc1 .Llight_path
	s_setprio 1
	s_mov_b32 s12, 0xbeb17218
	v_add_u32_e32 v3, 0x7800, v228
	ds_read2_b32 v[138:139], v3 offset0:16 offset1:48
	ds_read_b128 v[18:21], v2 offset:36928
	ds_read_b128 v[22:25], v2 offset:36944
	s_waitcnt lgkmcnt(2)
	v_add_u32_e32 v3, v230, v138
	ds_read_b128 v[26:29], v2 offset:36960
	ds_read_b128 v[30:33], v2 offset:36976
	ds_read_b128 v[142:145], v3 offset:16384
	ds_read_b128 v[130:133], v3 offset:16416
	ds_read_b128 v[154:157], v3 offset:16448
	ds_read_b128 v[134:137], v3 offset:16480
	ds_read_b128 v[248:251], v2 offset:37104
	ds_read_b128 v[244:247], v2 offset:37088
	ds_read_b128 v[240:243], v2 offset:37072
	ds_read_b128 v[236:239], v2 offset:37056
	s_waitcnt vmcnt(17) lgkmcnt(7)
	v_mfma_f32_32x32x16_bf16 v[18:33], v[94:97], v[142:145], v[18:33]
	s_waitcnt lgkmcnt(6)
	v_mfma_f32_32x32x16_bf16 v[18:33], v[90:93], v[130:133], v[18:33]
	s_waitcnt lgkmcnt(5)
	v_mfma_f32_32x32x16_bf16 v[18:33], v[86:89], v[154:157], v[18:33]
	s_waitcnt lgkmcnt(4)
	v_mfma_f32_32x32x16_bf16 v[18:33], v[82:85], v[134:137], v[18:33]
	s_cmpk_lt_u32 s19, 0x100
	s_cselect_b64 s[2:3], -1, 0
	ds_read_b32 v158, v228 offset:31040
	v_add_u32_e32 v159, v230, v139
	s_nop 2
	v_exp_f32_e32 v139, v20
	v_exp_f32_e32 v138, v24
	v_exp_f32_e32 v141, v28
	v_exp_f32_e32 v140, v32
	v_exp_f32_e32 v18, v18
	v_exp_f32_e32 v20, v22
	v_exp_f32_e32 v22, v26
	v_add_f32_e32 v24, 1.0, v138
	v_add_f32_e32 v26, 1.0, v141
	v_add_f32_e32 v19, 1.0, v139
	v_exp_f32_e32 v23, v30
	v_add_f32_e32 v27, 1.0, v140
	v_fmac_f32_e32 v24, v20, v24
	v_fmac_f32_e32 v26, v22, v26
	v_fmac_f32_e32 v19, v18, v19
	v_fmac_f32_e32 v27, v23, v27
	v_rcp_f32_e32 v18, v24
	v_rcp_f32_e32 v22, v27
	v_rcp_f32_e32 v19, v19
	v_rcp_f32_e32 v23, v26
	v_exp_f32_e32 v146, v21
	v_exp_f32_e32 v147, v25
	s_mov_b32 s8, 0xc038aa3b
	s_mov_b32 s4, 0x4038aa3b
	v_mov_b64_e32 v[160:161], s[8:9]
	v_exp_f32_e32 v148, v29
	v_exp_f32_e32 v149, v33
	v_pk_fma_f32 v[20:21], v[138:139], s[4:5], v[160:161] op_sel_hi:[1,0,0]
	s_nop 0
	v_pk_mul_f32 v[214:215], v[20:21], v[18:19]
	v_pk_fma_f32 v[18:19], v[140:141], s[4:5], v[160:161] op_sel_hi:[1,0,0]
	s_nop 0
	v_pk_mul_f32 v[212:213], v[18:19], v[22:23]
	v_add_u32_e32 v231, s7, v229
	ds_read_b128 v[18:21], v231 offset:36928
	ds_read_b128 v[22:25], v231 offset:36944
	ds_read_b128 v[26:29], v231 offset:36960
	ds_read_b128 v[30:33], v231 offset:36976
	s_waitcnt lgkmcnt(5)
	v_mfma_f32_32x32x16_bf16 v[2:17], v[46:49], v[142:145], v[236:251]
	ds_read_b128 v[138:141], v159 offset:16384
	v_add_f32_e32 v162, 1.0, v146
	v_exp_f32_e32 v163, v215
	v_exp_f32_e32 v164, v214
	v_exp_f32_e32 v165, v213
	v_exp_f32_e32 v166, v212
	v_add_f32_e32 v142, 1.0, v147
	v_add_f32_e32 v143, 1.0, v148
	v_add_f32_e32 v144, 1.0, v149
	v_mfma_f32_32x32x16_bf16 v[2:17], v[42:45], v[130:133], v[2:17]
	ds_read_b128 v[146:149], v159 offset:16416
	v_fmac_f32_e32 v162, v162, v163
	v_fmac_f32_e32 v142, v142, v164
	v_fmac_f32_e32 v143, v143, v165
	v_fmac_f32_e32 v144, v144, v166
	v_mfma_f32_32x32x16_bf16 v[2:17], v[38:41], v[154:157], v[2:17]
	ds_read_b128 v[150:153], v159 offset:16448
	v_rcp_f32_e32 v130, v162
	v_rcp_f32_e32 v131, v142
	v_rcp_f32_e32 v132, v143
	v_rcp_f32_e32 v133, v144
	s_waitcnt vmcnt(16)
	v_mfma_f32_32x32x16_bf16 v[2:17], v[34:37], v[134:137], v[2:17]
	ds_read_b128 v[178:181], v159 offset:16480
	v_fma_f32 v130, -v163, v130, v130
	v_fma_f32 v131, -v164, v131, v131
	v_fma_f32 v132, -v165, v132, v132
	v_fma_f32 v133, -v166, v133, v133
	v_add_u32_e32 v211, s6, v210
	v_cvt_pk_bf16_f32 v252, v130, v131
	v_cvt_pk_bf16_f32 v253, v132, v133
	s_nop 3
	v_exp_f32_e32 v131, v4
	v_exp_f32_e32 v130, v8
	v_exp_f32_e32 v133, v12
	v_exp_f32_e32 v132, v16
	v_exp_f32_e32 v2, v2
	v_exp_f32_e32 v4, v6
	v_exp_f32_e32 v6, v10
	v_exp_f32_e32 v7, v14
	v_add_f32_e32 v3, 1.0, v131
	v_add_f32_e32 v8, 1.0, v130
	v_add_f32_e32 v10, 1.0, v133
	v_add_f32_e32 v11, 1.0, v132
	v_fmac_f32_e32 v3, v2, v3
	v_fmac_f32_e32 v8, v4, v8
	v_fmac_f32_e32 v10, v6, v10
	v_fmac_f32_e32 v11, v7, v11
	v_rcp_f32_e32 v3, v3
	v_rcp_f32_e32 v2, v8
	v_rcp_f32_e32 v7, v10
	v_rcp_f32_e32 v6, v11
	v_exp_f32_e32 v134, v5
	v_exp_f32_e32 v135, v9
	v_pk_fma_f32 v[4:5], v[130:131], s[4:5], v[160:161] op_sel_hi:[1,0,0]
	v_exp_f32_e32 v130, v13
	v_pk_mul_f32 v[204:205], v[4:5], v[2:3]
	v_pk_fma_f32 v[2:3], v[132:133], s[4:5], v[160:161] op_sel_hi:[1,0,0]
	v_exp_f32_e32 v131, v17
	v_pk_mul_f32 v[202:203], v[2:3], v[6:7]
	s_waitcnt lgkmcnt(3)
	v_mfma_f32_32x32x16_bf16 v[18:33], v[94:97], v[138:141], v[18:33]
	v_add_f32_e32 v132, 1.0, v134
	v_exp_f32_e32 v133, v205
	v_add_f32_e32 v134, 1.0, v135
	v_exp_f32_e32 v135, v204
	v_exp_f32_e32 v136, v203
	v_exp_f32_e32 v137, v202
	v_add_f32_e32 v130, 1.0, v130
	v_add_f32_e32 v131, 1.0, v131
	s_waitcnt lgkmcnt(2)
	v_mfma_f32_32x32x16_bf16 v[18:33], v[90:93], v[146:149], v[18:33]
	v_fmac_f32_e32 v132, v132, v133
	v_fmac_f32_e32 v134, v134, v135
	v_fmac_f32_e32 v130, v130, v136
	v_fmac_f32_e32 v131, v131, v137
	s_waitcnt lgkmcnt(1)
	v_mfma_f32_32x32x16_bf16 v[18:33], v[86:89], v[150:153], v[18:33]
	v_rcp_f32_e32 v132, v132
	v_rcp_f32_e32 v134, v134
	v_rcp_f32_e32 v130, v130
	v_rcp_f32_e32 v131, v131
	s_waitcnt lgkmcnt(0)
	v_mfma_f32_32x32x16_bf16 v[18:33], v[82:85], v[178:181], v[18:33]
	v_fma_f32 v132, -v133, v132, v132
	v_fma_f32 v133, -v135, v134, v134
	v_fma_f32 v134, -v136, v130, v130
	v_fma_f32 v131, -v137, v131, v131
	v_cvt_pk_bf16_f32 v254, v132, v133
	v_cvt_pk_bf16_f32 v255, v134, v131
	ds_write_b128 v211, v[252:255] offset:0
	s_waitcnt lgkmcnt(0)
	s_barrier
	s_load_dwordx8 s[4:11], s[0:1], 0x10
	ds_read_b32 v229, v228 offset:31168
	ds_read_b128 v[174:177], v210
	v_add_u32_e32 v183, v230, v158
	ds_read_b128 v[170:173], v210 offset:1024
	v_exp_f32_e32 v131, v20
	v_exp_f32_e32 v130, v24
	v_exp_f32_e32 v133, v28
	v_exp_f32_e32 v132, v32
	ds_read_b128 v[166:169], v210 offset:2048
	v_exp_f32_e32 v18, v18
	v_exp_f32_e32 v20, v22
	v_exp_f32_e32 v22, v26
	v_exp_f32_e32 v23, v30
	v_fma_f32 v19, v131, s12, s12
	v_fma_f32 v24, v130, s12, s12
	v_fma_f32 v26, v133, s12, s12
	v_fma_f32 v27, v132, s12, s12
	ds_read_b128 v[162:165], v210 offset:3072
	v_fmac_f32_e32 v19, v18, v19
	v_fmac_f32_e32 v24, v20, v24
	v_fmac_f32_e32 v26, v22, v26
	v_fmac_f32_e32 v27, v23, v27
	ds_read_b128 v[158:161], v210 offset:4096
	v_rcp_f32_e32 v19, v19
	v_rcp_f32_e32 v18, v24
	v_rcp_f32_e32 v23, v26
	v_rcp_f32_e32 v22, v27
	ds_read_b128 v[154:157], v210 offset:5120
	v_exp_f32_e32 v186, v21
	v_exp_f32_e32 v187, v25
	ds_read_b128 v[142:145], v210 offset:6144
	s_mov_b32 s0, 0xc038aa3b
	v_exp_f32_e32 v188, v29
	v_pk_fma_f32 v[200:201], v[130:131], v[18:19], v[18:19] neg_lo:[1,0,0] neg_hi:[1,0,0]
	v_exp_f32_e32 v189, v33
	v_pk_fma_f32 v[198:199], v[132:133], v[22:23], v[22:23] neg_lo:[1,0,0] neg_hi:[1,0,0]
	ds_read_b128 v[130:133], v210 offset:7168
	ds_read_b128 v[18:21], v231 offset:36928
	ds_read_b128 v[22:25], v231 offset:36944
	ds_read_b128 v[26:29], v231 offset:36960
	ds_read_b128 v[30:33], v231 offset:36976
	v_mfma_f32_32x32x16_bf16 v[2:17], v[46:49], v[138:141], v[236:251]
	ds_read_b128 v[134:137], v183 offset:16384
	v_add_f32_e32 v186, 1.0, v186
	v_exp_f32_e32 v190, v201
	v_exp_f32_e32 v191, v200
	v_exp_f32_e32 v192, v199
	v_exp_f32_e32 v193, v198
	v_add_f32_e32 v187, 1.0, v187
	v_add_f32_e32 v188, 1.0, v188
	v_add_f32_e32 v189, 1.0, v189
	v_mfma_f32_32x32x16_bf16 v[2:17], v[42:45], v[146:149], v[2:17]
	ds_read_b128 v[138:141], v183 offset:16416
	v_fmac_f32_e32 v186, v186, v190
	v_fmac_f32_e32 v187, v187, v191
	v_fmac_f32_e32 v188, v188, v192
	v_fmac_f32_e32 v189, v189, v193
	v_mfma_f32_32x32x16_bf16 v[2:17], v[38:41], v[150:153], v[2:17]
	ds_read_b128 v[146:149], v183 offset:16448
	v_rcp_f32_e32 v186, v186
	v_rcp_f32_e32 v187, v187
	v_rcp_f32_e32 v188, v188
	v_rcp_f32_e32 v189, v189
	v_mfma_f32_32x32x16_bf16 v[2:17], v[34:37], v[178:181], v[2:17]
	ds_read_b128 v[150:153], v183 offset:16480
	v_fma_f32 v183, -v190, v186, v186
	v_fma_f32 v186, -v191, v187, v187
	v_fma_f32 v187, -v192, v188, v188
	v_fma_f32 v188, -v193, v189, v189
	s_waitcnt vmcnt(15) lgkmcnt(0)
	v_mfma_f32_32x32x16_bf16 v[18:33], v[126:129], v[174:177], v[18:33]
	v_cvt_pk_bf16_f32 v252, v183, v186
	v_cvt_pk_bf16_f32 v253, v187, v188
	s_waitcnt vmcnt(14)
	v_mfma_f32_32x32x16_bf16 v[18:33], v[122:125], v[170:173], v[18:33]
	s_nop 0
	v_exp_f32_e32 v179, v4
	v_exp_f32_e32 v178, v8
	v_exp_f32_e32 v181, v12
	v_exp_f32_e32 v180, v16
	s_waitcnt vmcnt(13)
	v_mfma_f32_32x32x16_bf16 v[18:33], v[118:121], v[166:169], v[18:33]
	v_exp_f32_e32 v2, v2
	v_exp_f32_e32 v4, v6
	v_exp_f32_e32 v7, v10
	v_exp_f32_e32 v8, v14
	v_fma_f32 v3, v179, s12, s12
	v_fma_f32 v6, v178, s12, s12
	v_fma_f32 v10, v181, s12, s12
	v_fma_f32 v11, v180, s12, s12
	s_waitcnt vmcnt(12)
	v_mfma_f32_32x32x16_bf16 v[18:33], v[114:117], v[162:165], v[18:33]
	v_fmac_f32_e32 v3, v2, v3
	v_fmac_f32_e32 v6, v4, v6
	v_fmac_f32_e32 v10, v7, v10
	v_fmac_f32_e32 v11, v8, v11
	s_waitcnt vmcnt(11)
	v_mfma_f32_32x32x16_bf16 v[18:33], v[110:113], v[158:161], v[18:33]
	v_rcp_f32_e32 v3, v3
	v_rcp_f32_e32 v2, v6
	v_rcp_f32_e32 v7, v10
	v_rcp_f32_e32 v6, v11
	s_waitcnt vmcnt(10)
	v_mfma_f32_32x32x16_bf16 v[18:33], v[106:109], v[154:157], v[18:33]
	v_exp_f32_e32 v183, v5
	v_exp_f32_e32 v186, v9
	s_waitcnt vmcnt(9)
	v_mfma_f32_32x32x16_bf16 v[18:33], v[102:105], v[142:145], v[18:33]
	v_pk_fma_f32 v[206:207], v[178:179], v[2:3], v[2:3] neg_lo:[1,0,0] neg_hi:[1,0,0]
	v_exp_f32_e32 v178, v13
	v_exp_f32_e32 v179, v17
	v_pk_fma_f32 v[208:209], v[180:181], v[6:7], v[6:7] neg_lo:[1,0,0] neg_hi:[1,0,0]
	s_waitcnt vmcnt(8)
	v_mfma_f32_32x32x16_bf16 v[18:33], v[98:101], v[130:133], v[18:33]
	v_mfma_f32_32x32x16_bf16 v[18:33], v[94:97], v[134:137], v[18:33]
	v_add_f32_e32 v180, 1.0, v183
	v_exp_f32_e32 v181, v207
	v_add_f32_e32 v183, 1.0, v186
	v_exp_f32_e32 v184, v206
	v_exp_f32_e32 v185, v209
	v_exp_f32_e32 v186, v208
	v_add_f32_e32 v178, 1.0, v178
	v_add_f32_e32 v179, 1.0, v179
	v_mfma_f32_32x32x16_bf16 v[18:33], v[90:93], v[138:141], v[18:33]
	v_fmac_f32_e32 v180, v180, v181
	v_fmac_f32_e32 v183, v183, v184
	v_fmac_f32_e32 v178, v178, v185
	v_fmac_f32_e32 v179, v179, v186
	v_mfma_f32_32x32x16_bf16 v[18:33], v[86:89], v[146:149], v[18:33]
	v_rcp_f32_e32 v180, v180
	v_rcp_f32_e32 v183, v183
	v_rcp_f32_e32 v178, v178
	v_rcp_f32_e32 v179, v179
	v_mfma_f32_32x32x16_bf16 v[18:33], v[82:85], v[150:153], v[18:33]
	v_fma_f32 v180, -v181, v180, v180
	v_fma_f32 v181, -v184, v183, v183
	v_fma_f32 v183, -v185, v178, v178
	v_fma_f32 v179, -v186, v179, v179
	v_cvt_pk_bf16_f32 v254, v180, v181
	v_cvt_pk_bf16_f32 v255, v183, v179
	ds_write_b128 v211, v[252:255] offset:8192
	s_waitcnt lgkmcnt(0)
	s_barrier
	v_mov_b32_e32 v178, 0x7a40
	v_lshl_add_u32 v232, v182, 2, v178
	s_mov_b32 s1, -1
	s_waitcnt vmcnt(0)
	s_branch .LBB1_14
	.p2align 6
